# v27
# speedup vs baseline: 1.0065x; 1.0048x over previous
.LBB1_12:
	s_waitcnt vmcnt(8)
	s_waitcnt lgkmcnt(0)
	s_barrier
	v_mfma_f32_16x16x32_f16 v[128:131], v[148:151], v[166:169], v[128:131]
	v_mfma_f32_16x16x32_f16 v[128:131], v[152:155], v[174:177], v[128:131]
	v_mfma_f32_16x16x32_f16 v[120:123], v[160:163], v[174:177], v[120:123]
	v_mfma_f32_16x16x32_f16 v[120:123], v[156:159], v[166:169], v[120:123]
	v_mfma_f32_16x16x32_f16 v[104:107], v[156:159], v[170:173], v[104:107]
	v_mfma_f32_16x16x32_f16 v[104:107], v[160:163], v[178:181], v[104:107]
	v_mfma_f32_16x16x32_f16 v[112:115], v[152:155], v[178:181], v[112:115]
	v_mfma_f32_16x16x32_f16 v[112:115], v[148:151], v[170:173], v[112:115]
	v_mfma_f32_16x16x32_f16 v[96:99], v[148:151], v[182:185], v[96:99]
	v_mfma_f32_16x16x32_f16 v[96:99], v[152:155], v[190:193], v[96:99]
	v_mfma_f32_16x16x32_f16 v[88:91], v[160:163], v[190:193], v[88:91]
	v_mfma_f32_16x16x32_f16 v[88:91], v[156:159], v[182:185], v[88:91]
	v_mfma_f32_16x16x32_f16 v[72:75], v[156:159], v[186:189], v[72:75]
	v_mfma_f32_16x16x32_f16 v[72:75], v[160:163], v[214:217], v[72:75]
	v_mfma_f32_16x16x32_f16 v[80:83], v[152:155], v[214:217], v[80:83]
	v_mfma_f32_16x16x32_f16 v[80:83], v[148:151], v[186:189], v[80:83]
	v_mfma_f32_16x16x32_f16 v[124:127], v[132:135], v[166:169], v[124:127]
	v_mfma_f32_16x16x32_f16 v[124:127], v[136:139], v[174:177], v[124:127]
	v_mfma_f32_16x16x32_f16 v[116:119], v[144:147], v[174:177], v[116:119]
	v_mfma_f32_16x16x32_f16 v[116:119], v[140:143], v[166:169], v[116:119]
	v_mfma_f32_16x16x32_f16 v[100:103], v[140:143], v[170:173], v[100:103]
	v_mfma_f32_16x16x32_f16 v[100:103], v[144:147], v[178:181], v[100:103]
	v_mfma_f32_16x16x32_f16 v[108:111], v[136:139], v[178:181], v[108:111]
	v_mfma_f32_16x16x32_f16 v[108:111], v[132:135], v[170:173], v[108:111]
	v_mfma_f32_16x16x32_f16 v[92:95], v[132:135], v[182:185], v[92:95]
	v_mfma_f32_16x16x32_f16 v[92:95], v[136:139], v[190:193], v[92:95]
	v_mfma_f32_16x16x32_f16 v[84:87], v[144:147], v[190:193], v[84:87]
	v_mfma_f32_16x16x32_f16 v[84:87], v[140:143], v[182:185], v[84:87]
	v_mfma_f32_16x16x32_f16 v[68:71], v[140:143], v[186:189], v[68:71]
	v_mfma_f32_16x16x32_f16 v[68:71], v[144:147], v[214:217], v[68:71]
	v_mfma_f32_16x16x32_f16 v[76:79], v[136:139], v[214:217], v[76:79]
	v_mfma_f32_16x16x32_f16 v[76:79], v[132:135], v[186:189], v[76:79]
	s_barrier
	ds_read_b128 v[188:191], v226 offset:16384
	ds_read_b128 v[176:179], v226 offset:18432
	ds_read_b128 v[192:195], v227 offset:16384
	ds_read_b128 v[180:183], v227 offset:18432
	ds_read_b128 v[172:175], v226 offset:20480
	ds_read_b128 v[164:167], v226 offset:22528
	ds_read_b128 v[184:187], v227 offset:20480
	ds_read_b128 v[168:171], v227 offset:22528
	s_andn2_b64 vcc, exec, s[4:5]
	s_cbranch_vccnz .LBB1_16
	v_cvt_pkrtz_f16_f32 v0, v0, v1
	v_cvt_pkrtz_f16_f32 v1, v2, v3
	v_add_u32_e32 v0, 0x20002, v0
	v_add_u32_e32 v1, 0x20002, v1
	v_and_b32_e32 v0, 0xfffcfffc, v0
	v_and_b32_e32 v1, 0xfffcfffc, v1
	global_store_dwordx2 v231, v[0:1], s[90:91]
.LBB1_16:
	s_add_u32 s28, s44, 0xfff00080
	s_addc_u32 s46, s45, -1
	s_cmp_eq_u32 s48, 60
	s_cselect_b32 s49, s31, s46
	s_cselect_b32 s47, s35, s81
	s_cselect_b32 s46, s78, s80
	s_mov_b32 m0, s52
	s_cselect_b32 s48, s77, s28
	s_add_u32 s50, s46, 0x100000
	global_load_lds_dwordx4 v200, s[46:47]
	s_mov_b32 m0, s53
	s_addc_u32 s51, s47, 0
	global_load_lds_dwordx4 v196, s[46:47]
	s_mov_b32 m0, s55
	s_add_u32 s84, s46, 0x80
	s_addc_u32 s85, s47, 0
	global_load_lds_dwordx4 v200, s[50:51]
	s_mov_b32 m0, s56
	s_add_u32 s86, s48, 0x80
	s_addc_u32 s87, s49, 0
	s_and_b64 s[4:5], exec, s[4:5]
	global_load_lds_dwordx4 v196, s[50:51]
	s_mov_b32 m0, s43
	s_mov_b64 s[50:51], -1
	global_load_lds_dwordx4 v202, s[48:49]
	s_mov_b32 m0, s54
	s_mov_b64 vcc, s[4:5]
	global_load_lds_dwordx4 v198, s[48:49]
	s_cbranch_vccz .LBB1_18
	s_waitcnt vmcnt(8)
	s_mov_b64 s[50:51], 0
